# v63 with the static s_setprio 1 on waves 0-3 (older half) instead of waves 4-7
# speedup vs baseline: 1.0055x; 1.0055x over previous
_Z8mega_fwd5FArgs:
	v_readfirstlane_b32 s98, v0
	s_nop 0
	s_bitcmp0_b32 s98, 8
	s_cbranch_scc0 .Lprio_skip
	s_setprio 1
